# v16
# baseline (speedup 1.0000x reference)
.LBB2_63:
	v_lshrrev_b32_e32 v69, 5, v68
	v_lshlrev_b32_e32 v90, 8, v75
	v_xor_b32_e32 v2, v69, v73
	v_lshl_or_b32 v92, v2, 4, v90
	v_or_b32_e32 v6, 32, v75
	v_min_i32_e32 v75, 59, v6
	v_lshlrev_b32_e32 v91, 8, v75
	v_bitop3_b32 v6, v69, v75, 15 bitop3:0x78
	v_lshl_or_b32 v93, v6, 4, v91
	s_waitcnt lgkmcnt(0)
	s_barrier
	ds_read_b128 v[76:79], v92
	ds_read_b128 v[80:83], v93
	v_xor_b32_e32 v84, 32, v92
	v_xor_b32_e32 v88, 32, v93
	ds_read_b128 v[84:87], v84
	ds_read_b128 v[88:91], v88
	s_waitcnt vmcnt(7) lgkmcnt(2)
	v_mfma_f32_32x32x16_f16 v[18:33], v[76:79], v[46:49], 0
	v_mfma_f32_32x32x16_f16 v[2:17], v[80:83], v[46:49], 0
	s_mov_b32 s0, 0x9000
	v_add_co_u32_e32 v94, vcc, s0, v70
	v_xor_b32_e32 v76, 64, v92
	v_xor_b32_e32 v80, 64, v93
	v_addc_co_u32_e32 v95, vcc, 0, v71, vcc
	global_load_dwordx4 v[46:49], v[94:95], off offset:-4096
	ds_read_b128 v[76:79], v76
	ds_read_b128 v[80:83], v80
	s_waitcnt vmcnt(7) lgkmcnt(2)
	v_mfma_f32_32x32x16_f16 v[18:33], v[84:87], v[34:37], v[18:33]
	v_mfma_f32_32x32x16_f16 v[2:17], v[88:91], v[34:37], v[2:17]
	v_xor_b32_e32 v84, 0x60, v92
	v_xor_b32_e32 v88, 0x60, v93
	global_load_dwordx4 v[34:37], v[94:95], off
	ds_read_b128 v[84:87], v84
	ds_read_b128 v[88:91], v88
	s_waitcnt vmcnt(7) lgkmcnt(2)
	v_mfma_f32_32x32x16_f16 v[18:33], v[76:79], v[54:57], v[18:33]
	v_mfma_f32_32x32x16_f16 v[2:17], v[80:83], v[54:57], v[2:17]
	s_mov_b32 s0, 0xb000
	v_add_co_u32_e32 v94, vcc, s0, v70
	v_xor_b32_e32 v76, 0x80, v92
	v_xor_b32_e32 v80, 0x80, v93
	v_addc_co_u32_e32 v95, vcc, 0, v71, vcc
	global_load_dwordx4 v[54:57], v[94:95], off offset:-4096
	ds_read_b128 v[76:79], v76
	ds_read_b128 v[80:83], v80
	s_waitcnt vmcnt(7) lgkmcnt(2)
	v_mfma_f32_32x32x16_f16 v[18:33], v[84:87], v[38:41], v[18:33]
	v_mfma_f32_32x32x16_f16 v[2:17], v[88:91], v[38:41], v[2:17]
	v_xor_b32_e32 v84, 0xa0, v92
	v_xor_b32_e32 v88, 0xa0, v93
	global_load_dwordx4 v[38:41], v[94:95], off
	ds_read_b128 v[84:87], v84
	ds_read_b128 v[88:91], v88
	s_waitcnt vmcnt(7) lgkmcnt(2)
	v_mfma_f32_32x32x16_f16 v[18:33], v[76:79], v[62:65], v[18:33]
	v_mfma_f32_32x32x16_f16 v[2:17], v[80:83], v[62:65], v[2:17]
	s_mov_b32 s0, 0xd000
	v_add_co_u32_e32 v94, vcc, s0, v70
	v_xor_b32_e32 v76, 0xc0, v92
	v_xor_b32_e32 v80, 0xc0, v93
	v_addc_co_u32_e32 v95, vcc, 0, v71, vcc
	global_load_dwordx4 v[62:65], v[94:95], off offset:-4096
	ds_read_b128 v[76:79], v76
	ds_read_b128 v[80:83], v80
	s_waitcnt vmcnt(7) lgkmcnt(2)
	v_mfma_f32_32x32x16_f16 v[18:33], v[84:87], v[42:45], v[18:33]
	v_mfma_f32_32x32x16_f16 v[2:17], v[88:91], v[42:45], v[2:17]
	v_xor_b32_e32 v84, 0xe0, v92
	v_xor_b32_e32 v88, 0xe0, v93
	global_load_dwordx4 v[42:45], v[94:95], off
	ds_read_b128 v[84:87], v84
	ds_read_b128 v[88:91], v88
	s_waitcnt vmcnt(7) lgkmcnt(2)
	v_mfma_f32_32x32x16_f16 v[18:33], v[76:79], v[58:61], v[18:33]
	v_mfma_f32_32x32x16_f16 v[2:17], v[80:83], v[58:61], v[2:17]
	s_mov_b32 s0, 0xf000
	v_add_co_u32_e32 v94, vcc, s0, v70
	v_mov_b32_e32 v76, v92
	v_mov_b32_e32 v80, v93
	v_addc_co_u32_e32 v95, vcc, 0, v71, vcc
	global_load_dwordx4 v[58:61], v[94:95], off offset:-4096
	ds_read_b128 v[76:79], v76 offset:15360
	ds_read_b128 v[80:83], v80 offset:15360
	s_waitcnt vmcnt(7) lgkmcnt(2)
	v_mfma_f32_32x32x16_f16 v[18:33], v[84:87], v[50:53], v[18:33]
	v_mfma_f32_32x32x16_f16 v[2:17], v[88:91], v[50:53], v[2:17]
	v_xor_b32_e32 v84, 32, v92
	v_xor_b32_e32 v88, 32, v93
	global_load_dwordx4 v[50:53], v[94:95], off
	ds_read_b128 v[84:87], v84 offset:15360
	ds_read_b128 v[88:91], v88 offset:15360
	s_waitcnt vmcnt(7) lgkmcnt(2)
	v_mfma_f32_32x32x16_f16 v[18:33], v[76:79], v[46:49], v[18:33]
	v_mfma_f32_32x32x16_f16 v[2:17], v[80:83], v[46:49], v[2:17]
	v_xor_b32_e32 v76, 64, v92
	v_xor_b32_e32 v80, 64, v93
	ds_read_b128 v[76:79], v76 offset:15360
	ds_read_b128 v[80:83], v80 offset:15360
	s_waitcnt vmcnt(6) lgkmcnt(2)
	v_mfma_f32_32x32x16_f16 v[18:33], v[84:87], v[34:37], v[18:33]
	v_mfma_f32_32x32x16_f16 v[2:17], v[88:91], v[34:37], v[2:17]
	v_xor_b32_e32 v84, 0x60, v92
	v_xor_b32_e32 v88, 0x60, v93
	ds_read_b128 v[84:87], v84 offset:15360
	ds_read_b128 v[88:91], v88 offset:15360
	s_waitcnt vmcnt(5) lgkmcnt(2)
	v_mfma_f32_32x32x16_f16 v[18:33], v[76:79], v[54:57], v[18:33]
	v_mfma_f32_32x32x16_f16 v[2:17], v[80:83], v[54:57], v[2:17]
	v_xor_b32_e32 v76, 0x80, v92
	v_xor_b32_e32 v80, 0x80, v93
	ds_read_b128 v[76:79], v76 offset:15360
	ds_read_b128 v[80:83], v80 offset:15360
	s_waitcnt vmcnt(4) lgkmcnt(2)
	v_mfma_f32_32x32x16_f16 v[18:33], v[84:87], v[38:41], v[18:33]
	v_mfma_f32_32x32x16_f16 v[2:17], v[88:91], v[38:41], v[2:17]
	v_xor_b32_e32 v84, 0xa0, v92
	v_xor_b32_e32 v88, 0xa0, v93
	ds_read_b128 v[84:87], v84 offset:15360
	ds_read_b128 v[88:91], v88 offset:15360
	s_waitcnt vmcnt(3) lgkmcnt(2)
	v_mfma_f32_32x32x16_f16 v[18:33], v[76:79], v[62:65], v[18:33]
	v_mfma_f32_32x32x16_f16 v[2:17], v[80:83], v[62:65], v[2:17]
	v_xor_b32_e32 v76, 0xc0, v92
	v_xor_b32_e32 v80, 0xc0, v93
	ds_read_b128 v[76:79], v76 offset:15360
	ds_read_b128 v[80:83], v80 offset:15360
	s_waitcnt vmcnt(2) lgkmcnt(2)
	v_mfma_f32_32x32x16_f16 v[18:33], v[84:87], v[42:45], v[18:33]
	v_mfma_f32_32x32x16_f16 v[2:17], v[88:91], v[42:45], v[2:17]
	v_xor_b32_e32 v84, 0xe0, v92
	v_xor_b32_e32 v88, 0xe0, v93
	ds_read_b128 v[84:87], v84 offset:15360
	ds_read_b128 v[88:91], v88 offset:15360
	s_waitcnt vmcnt(1) lgkmcnt(2)
	v_mfma_f32_32x32x16_f16 v[18:33], v[76:79], v[58:61], v[18:33]
	v_mfma_f32_32x32x16_f16 v[2:17], v[80:83], v[58:61], v[2:17]
	v_lshlrev_b32_e32 v34, 1, v74
	s_movk_i32 s0, 0x440
	v_mad_u32_u24 v36, v69, s0, v34
	v_cmp_gt_u32_e32 vcc, 32, v68
	s_waitcnt lgkmcnt(0)
	s_barrier
	s_waitcnt vmcnt(0)
	v_mfma_f32_32x32x16_f16 v[18:33], v[84:87], v[50:53], v[18:33]
	v_mfma_f32_32x32x16_f16 v[2:17], v[88:91], v[50:53], v[2:17]
	s_nop 10
	v_add_f32_e32 v18, v67, v18
	v_max_f32_e32 v18, 0, v18
	v_add_f32_e32 v19, v67, v19
	v_cvt_f16_f32_e32 v35, v18
	v_max_f32_e32 v19, 0, v19
	v_cvt_f16_f32_e32 v19, v19
	v_add_f32_e32 v20, v67, v20
	v_add_f32_e32 v2, v67, v2
	v_max_f32_e32 v2, 0, v2
	v_cvt_f16_f32_e32 v2, v2
	v_add_f32_e32 v3, v67, v3
	v_max_f32_e32 v3, 0, v3
	v_cvt_f16_f32_e32 v3, v3
	v_max_f32_e32 v20, 0, v20
	v_cvt_f16_f32_e32 v20, v20
	ds_write_b16 v36, v35
	ds_write_b16 v36, v2 offset:8704
	ds_write_b16 v36, v19 offset:272
	ds_write_b16 v36, v3 offset:8976
	ds_write_b16 v36, v20 offset:544
	v_add_f32_e32 v2, v67, v4
	v_max_f32_e32 v2, 0, v2
	v_add_f32_e32 v3, v67, v21
	v_cvt_f16_f32_e32 v2, v2
	v_max_f32_e32 v3, 0, v3
	v_add_f32_e32 v4, v67, v5
	v_cvt_f16_f32_e32 v3, v3
	v_max_f32_e32 v4, 0, v4
	v_add_f32_e32 v5, v67, v22
	v_cvt_f16_f32_e32 v4, v4
	v_max_f32_e32 v5, 0, v5
	v_cvt_f16_f32_e32 v5, v5
	ds_write_b16 v36, v2 offset:9248
	ds_write_b16 v36, v3 offset:816
	ds_write_b16 v36, v4 offset:9520
	ds_write_b16 v36, v5 offset:2176
	v_add_f32_e32 v2, v67, v6
	v_max_f32_e32 v2, 0, v2
	v_add_f32_e32 v3, v67, v23
	v_cvt_f16_f32_e32 v2, v2
	v_max_f32_e32 v3, 0, v3
	v_add_f32_e32 v4, v67, v7
	v_cvt_f16_f32_e32 v3, v3
	v_max_f32_e32 v4, 0, v4
	v_add_f32_e32 v5, v67, v24
	v_cvt_f16_f32_e32 v4, v4
	v_max_f32_e32 v5, 0, v5
	v_cvt_f16_f32_e32 v5, v5
	ds_write_b16 v36, v2 offset:10880
	ds_write_b16 v36, v3 offset:2448
	ds_write_b16 v36, v4 offset:11152
	ds_write_b16 v36, v5 offset:2720
	v_add_f32_e32 v2, v67, v8
	v_max_f32_e32 v2, 0, v2
	v_add_f32_e32 v3, v67, v25
	v_cvt_f16_f32_e32 v2, v2
	v_max_f32_e32 v3, 0, v3
	v_add_f32_e32 v4, v67, v9
	v_cvt_f16_f32_e32 v3, v3
	v_max_f32_e32 v4, 0, v4
	v_add_f32_e32 v5, v67, v26
	v_cvt_f16_f32_e32 v4, v4
	v_max_f32_e32 v5, 0, v5
	v_cvt_f16_f32_e32 v5, v5
	ds_write_b16 v36, v2 offset:11424
	ds_write_b16 v36, v3 offset:2992
	ds_write_b16 v36, v4 offset:11696
	ds_write_b16 v36, v5 offset:4352
	v_add_f32_e32 v2, v67, v10
	v_max_f32_e32 v2, 0, v2
	v_add_f32_e32 v3, v67, v27
	v_cvt_f16_f32_e32 v2, v2
	v_max_f32_e32 v3, 0, v3
	v_add_f32_e32 v4, v67, v11
	v_cvt_f16_f32_e32 v3, v3
	v_max_f32_e32 v4, 0, v4
	v_add_f32_e32 v5, v67, v28
	v_cvt_f16_f32_e32 v4, v4
	v_max_f32_e32 v5, 0, v5
	v_cvt_f16_f32_e32 v5, v5
	ds_write_b16 v36, v2 offset:13056
	ds_write_b16 v36, v3 offset:4624
	ds_write_b16 v36, v4 offset:13328
	ds_write_b16 v36, v5 offset:4896
	v_add_f32_e32 v2, v67, v12
	v_max_f32_e32 v2, 0, v2
	v_add_f32_e32 v3, v67, v29
	v_cvt_f16_f32_e32 v2, v2
	v_max_f32_e32 v3, 0, v3
	v_add_f32_e32 v4, v67, v13
	v_cvt_f16_f32_e32 v3, v3
	v_max_f32_e32 v4, 0, v4
	v_add_f32_e32 v5, v67, v30
	v_cvt_f16_f32_e32 v4, v4
	v_max_f32_e32 v5, 0, v5
	v_mul_u32_u24_e32 v18, 0x440, v69
	v_cvt_f16_f32_e32 v5, v5
	ds_write_b16 v36, v2 offset:13600
	ds_write_b16 v36, v3 offset:5168
	ds_write_b16 v36, v4 offset:13872
	ds_write_b16 v36, v5 offset:6528
	s_and_saveexec_b64 s[0:1], vcc
	s_cbranch_execz .LBB2_65
	v_add_f32_e32 v2, v67, v14
	v_max_f32_e32 v2, 0, v2
	v_cvt_f16_f32_e32 v2, v2
	ds_write_b16 v34, v2 offset:15232

.LBB2_107:
	s_or_b64 exec, exec, s[2:3]
	s_load_dwordx4 s[4:7], s[0:1], 0x38
	s_cmpk_lt_i32 s19, 0x181
	s_cbranch_scc0 .LBB2_62
	s_branch .LBB2_63
	s_nop 0
	s_nop 0
	s_nop 0
	s_nop 0
	s_nop 0
	s_nop 0
	s_nop 0
	s_nop 0
	s_nop 0
	s_nop 0
	s_nop 0
	s_nop 0
	s_nop 0
	s_nop 0
	s_nop 0
	s_nop 0
	s_nop 0
	s_nop 0
	s_nop 0
	s_nop 0
	s_nop 0
	s_nop 0
	s_nop 0
	s_nop 0
	s_nop 0
	s_nop 0
	s_nop 0
	s_nop 0
	s_nop 0
	s_nop 0
	s_nop 0
	s_nop 0
	s_nop 0
	s_nop 0
	s_nop 0
	s_endpgm

	.amdhsa_kernel _Z7k_layerILb1EEvPKvPKhPKfPKiS7_PKDF16_S5_PvPhPf
		.amdhsa_group_segment_fixed_size 30720
		.amdhsa_private_segment_fixed_size 0
		.amdhsa_kernarg_size 80
		.amdhsa_user_sgpr_count 2
		.amdhsa_user_sgpr_dispatch_ptr 0
		.amdhsa_user_sgpr_queue_ptr 0
		.amdhsa_user_sgpr_kernarg_segment_ptr 1
		.amdhsa_user_sgpr_dispatch_id 0
		.amdhsa_user_sgpr_kernarg_preload_length 0
		.amdhsa_user_sgpr_kernarg_preload_offset 0
		.amdhsa_user_sgpr_private_segment_size 0
		.amdhsa_uses_dynamic_stack 0
		.amdhsa_enable_private_segment 0
		.amdhsa_system_sgpr_workgroup_id_x 1
		.amdhsa_system_sgpr_workgroup_id_y 0
		.amdhsa_system_sgpr_workgroup_id_z 0
		.amdhsa_system_sgpr_workgroup_info 0
		.amdhsa_system_vgpr_workitem_id 0
		.amdhsa_next_free_vgpr 96
		.amdhsa_next_free_sgpr 96
		.amdhsa_accum_offset 96
		.amdhsa_reserve_vcc 1
		.amdhsa_float_round_mode_32 0
		.amdhsa_float_round_mode_16_64 0
		.amdhsa_float_denorm_mode_32 3
		.amdhsa_float_denorm_mode_16_64 3
		.amdhsa_dx10_clamp 1
		.amdhsa_ieee_mode 1
		.amdhsa_fp16_overflow 0
		.amdhsa_tg_split 0
		.amdhsa_exception_fp_ieee_invalid_op 0
		.amdhsa_exception_fp_denorm_src 0
		.amdhsa_exception_fp_ieee_div_zero 0
		.amdhsa_exception_fp_ieee_overflow 0
		.amdhsa_exception_fp_ieee_underflow 0
		.amdhsa_exception_fp_ieee_inexact 0
		.amdhsa_exception_int_div_zero 0
	.end_amdhsa_kernel

.Lfunc_end2:
	.size	_Z7k_layerILb1EEvPKvPKhPKfPKiS7_PKDF16_S5_PvPhPf, .Lfunc_end2-_Z7k_layerILb1EEvPKvPKhPKfPKiS7_PKDF16_S5_PvPhPf
	.set _Z7k_layerILb1EEvPKvPKhPKfPKiS7_PKDF16_S5_PvPhPf.num_vgpr, 96
	.set _Z7k_layerILb1EEvPKvPKhPKfPKiS7_PKDF16_S5_PvPhPf.num_agpr, 0
	.set _Z7k_layerILb1EEvPKvPKhPKfPKiS7_PKDF16_S5_PvPhPf.numbered_sgpr, 30
	.set _Z7k_layerILb1EEvPKvPKhPKfPKiS7_PKDF16_S5_PvPhPf.num_named_barrier, 0
	.set _Z7k_layerILb1EEvPKvPKhPKfPKiS7_PKDF16_S5_PvPhPf.private_seg_size, 0
	.set _Z7k_layerILb1EEvPKvPKhPKfPKiS7_PKDF16_S5_PvPhPf.uses_vcc, 1
	.set _Z7k_layerILb1EEvPKvPKhPKfPKiS7_PKDF16_S5_PvPhPf.uses_flat_scratch, 0
	.set _Z7k_layerILb1EEvPKvPKhPKfPKiS7_PKDF16_S5_PvPhPf.has_dyn_sized_stack, 0
	.set _Z7k_layerILb1EEvPKvPKhPKfPKiS7_PKDF16_S5_PvPhPf.has_recursion, 0
	.set _Z7k_layerILb1EEvPKvPKhPKfPKiS7_PKDF16_S5_PvPhPf.has_indirect_call, 0

.LBB3_61:
	s_waitcnt vmcnt(8)
	v_lshrrev_b32_e32 v67, 5, v66
	v_lshlrev_b32_e32 v90, 8, v72
	v_xor_b32_e32 v2, v67, v71
	v_lshl_or_b32 v88, v2, 4, v90
	v_or_b32_e32 v6, 32, v72
	v_min_i32_e32 v72, 59, v6
	v_lshlrev_b32_e32 v91, 8, v72
	v_bitop3_b32 v6, v67, v72, 15 bitop3:0x78
	v_lshl_or_b32 v89, v6, 4, v91
	s_waitcnt lgkmcnt(0)
	s_barrier
	ds_read_b128 v[72:75], v88
	ds_read_b128 v[76:79], v89
	v_xor_b32_e32 v80, 32, v88
	v_xor_b32_e32 v84, 32, v89
	ds_read_b128 v[80:83], v80
	ds_read_b128 v[84:87], v84
	s_waitcnt vmcnt(7) lgkmcnt(2)
	v_mfma_f32_32x32x16_f16 v[18:33], v[72:75], v[46:49], 0
	v_mfma_f32_32x32x16_f16 v[2:17], v[76:79], v[46:49], 0
	s_mov_b32 s0, 0x9000
	v_add_co_u32_e32 v90, vcc, s0, v68
	v_xor_b32_e32 v72, 64, v88
	v_xor_b32_e32 v76, 64, v89
	v_addc_co_u32_e32 v91, vcc, 0, v69, vcc
	global_load_dwordx4 v[46:49], v[90:91], off offset:-4096
	ds_read_b128 v[72:75], v72
	ds_read_b128 v[76:79], v76
	s_waitcnt vmcnt(7) lgkmcnt(2)
	v_mfma_f32_32x32x16_f16 v[18:33], v[80:83], v[34:37], v[18:33]
	v_mfma_f32_32x32x16_f16 v[2:17], v[84:87], v[34:37], v[2:17]
	v_xor_b32_e32 v80, 0x60, v88
	v_xor_b32_e32 v84, 0x60, v89
	global_load_dwordx4 v[34:37], v[90:91], off
	ds_read_b128 v[80:83], v80
	ds_read_b128 v[84:87], v84
	s_waitcnt vmcnt(7) lgkmcnt(2)
	v_mfma_f32_32x32x16_f16 v[18:33], v[72:75], v[54:57], v[18:33]
	v_mfma_f32_32x32x16_f16 v[2:17], v[76:79], v[54:57], v[2:17]
	s_mov_b32 s0, 0xb000
	v_add_co_u32_e32 v90, vcc, s0, v68
	v_xor_b32_e32 v72, 0x80, v88
	v_xor_b32_e32 v76, 0x80, v89
	v_addc_co_u32_e32 v91, vcc, 0, v69, vcc
	global_load_dwordx4 v[54:57], v[90:91], off offset:-4096
	ds_read_b128 v[72:75], v72
	ds_read_b128 v[76:79], v76
	s_waitcnt vmcnt(7) lgkmcnt(2)
	v_mfma_f32_32x32x16_f16 v[18:33], v[80:83], v[38:41], v[18:33]
	v_mfma_f32_32x32x16_f16 v[2:17], v[84:87], v[38:41], v[2:17]
	v_xor_b32_e32 v80, 0xa0, v88
	v_xor_b32_e32 v84, 0xa0, v89
	global_load_dwordx4 v[38:41], v[90:91], off
	ds_read_b128 v[80:83], v80
	ds_read_b128 v[84:87], v84
	s_waitcnt vmcnt(7) lgkmcnt(2)
	v_mfma_f32_32x32x16_f16 v[18:33], v[72:75], v[58:61], v[18:33]
	v_mfma_f32_32x32x16_f16 v[2:17], v[76:79], v[58:61], v[2:17]
	s_mov_b32 s0, 0xd000
	v_add_co_u32_e32 v90, vcc, s0, v68
	v_xor_b32_e32 v72, 0xc0, v88
	v_xor_b32_e32 v76, 0xc0, v89
	v_addc_co_u32_e32 v91, vcc, 0, v69, vcc
	global_load_dwordx4 v[58:61], v[90:91], off offset:-4096
	ds_read_b128 v[72:75], v72
	ds_read_b128 v[76:79], v76
	s_waitcnt vmcnt(7) lgkmcnt(2)
	v_mfma_f32_32x32x16_f16 v[18:33], v[80:83], v[42:45], v[18:33]
	v_mfma_f32_32x32x16_f16 v[2:17], v[84:87], v[42:45], v[2:17]
	v_xor_b32_e32 v80, 0xe0, v88
	v_xor_b32_e32 v84, 0xe0, v89
	global_load_dwordx4 v[42:45], v[90:91], off
	ds_read_b128 v[80:83], v80
	ds_read_b128 v[84:87], v84
	s_waitcnt vmcnt(7) lgkmcnt(2)
	v_mfma_f32_32x32x16_f16 v[18:33], v[72:75], v[62:65], v[18:33]
	v_mfma_f32_32x32x16_f16 v[2:17], v[76:79], v[62:65], v[2:17]
	s_mov_b32 s0, 0xf000
	v_add_co_u32_e32 v90, vcc, s0, v68
	v_mov_b32_e32 v72, v88
	v_mov_b32_e32 v76, v89
	v_addc_co_u32_e32 v91, vcc, 0, v69, vcc
	global_load_dwordx4 v[62:65], v[90:91], off offset:-4096
	ds_read_b128 v[72:75], v72 offset:15360
	ds_read_b128 v[76:79], v76 offset:15360
	s_waitcnt vmcnt(7) lgkmcnt(2)
	v_mfma_f32_32x32x16_f16 v[18:33], v[80:83], v[50:53], v[18:33]
	v_mfma_f32_32x32x16_f16 v[2:17], v[84:87], v[50:53], v[2:17]
	v_xor_b32_e32 v80, 32, v88
	v_xor_b32_e32 v84, 32, v89
	global_load_dwordx4 v[50:53], v[90:91], off
	ds_read_b128 v[80:83], v80 offset:15360
	ds_read_b128 v[84:87], v84 offset:15360
	s_waitcnt vmcnt(7) lgkmcnt(2)
	v_mfma_f32_32x32x16_f16 v[18:33], v[72:75], v[46:49], v[18:33]
	v_mfma_f32_32x32x16_f16 v[2:17], v[76:79], v[46:49], v[2:17]
	v_xor_b32_e32 v72, 64, v88
	v_xor_b32_e32 v76, 64, v89
	ds_read_b128 v[72:75], v72 offset:15360
	ds_read_b128 v[76:79], v76 offset:15360
	s_waitcnt vmcnt(6) lgkmcnt(2)
	v_mfma_f32_32x32x16_f16 v[18:33], v[80:83], v[34:37], v[18:33]
	v_mfma_f32_32x32x16_f16 v[2:17], v[84:87], v[34:37], v[2:17]
	v_xor_b32_e32 v80, 0x60, v88
	v_xor_b32_e32 v84, 0x60, v89
	ds_read_b128 v[80:83], v80 offset:15360
	ds_read_b128 v[84:87], v84 offset:15360
	s_waitcnt vmcnt(5) lgkmcnt(2)
	v_mfma_f32_32x32x16_f16 v[18:33], v[72:75], v[54:57], v[18:33]
	v_mfma_f32_32x32x16_f16 v[2:17], v[76:79], v[54:57], v[2:17]
	v_xor_b32_e32 v72, 0x80, v88
	v_xor_b32_e32 v76, 0x80, v89
	ds_read_b128 v[72:75], v72 offset:15360
	ds_read_b128 v[76:79], v76 offset:15360
	s_waitcnt vmcnt(4) lgkmcnt(2)
	v_mfma_f32_32x32x16_f16 v[18:33], v[80:83], v[38:41], v[18:33]
	v_mfma_f32_32x32x16_f16 v[2:17], v[84:87], v[38:41], v[2:17]
	v_xor_b32_e32 v80, 0xa0, v88
	v_xor_b32_e32 v84, 0xa0, v89
	ds_read_b128 v[80:83], v80 offset:15360
	ds_read_b128 v[84:87], v84 offset:15360
	s_waitcnt vmcnt(3) lgkmcnt(2)
	v_mfma_f32_32x32x16_f16 v[18:33], v[72:75], v[58:61], v[18:33]
	v_mfma_f32_32x32x16_f16 v[2:17], v[76:79], v[58:61], v[2:17]
	v_xor_b32_e32 v72, 0xc0, v88
	v_xor_b32_e32 v76, 0xc0, v89
	ds_read_b128 v[72:75], v72 offset:15360
	ds_read_b128 v[76:79], v76 offset:15360
	s_waitcnt vmcnt(2) lgkmcnt(2)
	v_mfma_f32_32x32x16_f16 v[18:33], v[80:83], v[42:45], v[18:33]
	v_mfma_f32_32x32x16_f16 v[2:17], v[84:87], v[42:45], v[2:17]
	v_xor_b32_e32 v80, 0xe0, v88
	v_xor_b32_e32 v84, 0xe0, v89
	ds_read_b128 v[80:83], v80 offset:15360
	ds_read_b128 v[84:87], v84 offset:15360
	s_waitcnt vmcnt(1) lgkmcnt(2)
	v_mfma_f32_32x32x16_f16 v[18:33], v[72:75], v[62:65], v[18:33]
	v_mfma_f32_32x32x16_f16 v[2:17], v[76:79], v[62:65], v[2:17]
	v_cmp_gt_u32_e32 vcc, 32, v66
	s_waitcnt lgkmcnt(0)
	s_barrier
	s_waitcnt vmcnt(0)
	v_mfma_f32_32x32x16_f16 v[18:33], v[80:83], v[50:53], v[18:33]
	v_mfma_f32_32x32x16_f16 v[2:17], v[84:87], v[50:53], v[2:17]
	s_nop 10
	v_add_f32_e32 v42, v70, v18
	v_lshlrev_b32_e32 v18, 11, v67
	v_or_b32_e32 v43, v1, v18
	v_add_f32_e32 v19, v70, v19
	ds_write2st64_b32 v43, v42, v19 offset1:2
	v_add_f32_e32 v19, v70, v20
	s_nop 6
	v_add_f32_e32 v3, v70, v3
	v_add_f32_e32 v4, v70, v4
	ds_write2st64_b32 v43, v3, v4 offset0:66 offset1:68
	v_add_f32_e32 v3, v70, v21
	ds_write2st64_b32 v43, v19, v3 offset0:4 offset1:6
	v_add_f32_e32 v3, v70, v5
	v_add_f32_e32 v5, v70, v6
	v_add_f32_e32 v4, v70, v22
	ds_write2st64_b32 v43, v3, v5 offset0:70 offset1:80
	v_add_f32_e32 v3, v70, v23
	ds_write2st64_b32 v43, v4, v3 offset0:16 offset1:18
	v_add_f32_e32 v3, v70, v7
	v_add_f32_e32 v5, v70, v8
	v_add_f32_e32 v4, v70, v24
	ds_write2st64_b32 v43, v3, v5 offset0:82 offset1:84
	v_add_f32_e32 v3, v70, v25
	ds_write2st64_b32 v43, v4, v3 offset0:20 offset1:22
	v_add_f32_e32 v3, v70, v9
	v_add_f32_e32 v5, v70, v10
	v_add_f32_e32 v4, v70, v26
	ds_write2st64_b32 v43, v3, v5 offset0:86 offset1:96
	v_add_f32_e32 v3, v70, v27
	ds_write2st64_b32 v43, v4, v3 offset0:32 offset1:34
	v_add_f32_e32 v3, v70, v11
	v_add_f32_e32 v5, v70, v12
	v_add_f32_e32 v4, v70, v28
	ds_write2st64_b32 v43, v3, v5 offset0:98 offset1:100
	v_add_f32_e32 v3, v70, v29
	ds_write2st64_b32 v43, v4, v3 offset0:36 offset1:38
	v_add_f32_e32 v3, v70, v13
	v_add_f32_e32 v2, v70, v2
	ds_write_b32 v43, v3 offset:26112
	v_add_f32_e32 v3, v70, v30
	ds_write2st64_b32 v43, v3, v2 offset0:48 offset1:64
	s_and_saveexec_b64 s[0:1], vcc
	v_add_f32_e32 v2, v70, v14
	ds_write_b32 v1, v2 offset:28672
	s_or_b64 exec, exec, s[0:1]
	v_lshlrev_b32_e32 v3, 2, v67
	v_add_f32_e32 v4, v70, v31
	v_add_u32_e32 v2, v1, v18
	ds_write_b32 v2, v4 offset:12800
	v_or_b32_e32 v4, 57, v3
	v_cmp_gt_u32_e64 s[0:1], 60, v4
	s_and_saveexec_b64 s[4:5], s[0:1]
	v_lshl_or_b32 v4, v4, 9, v1
	v_add_f32_e32 v5, v70, v15
	ds_write_b32 v4, v5
	s_or_b64 exec, exec, s[4:5]
	v_or_b32_e32 v3, 58, v3
	v_add_f32_e32 v4, v70, v32
	v_cmp_gt_u32_e64 s[0:1], 60, v3
	ds_write_b32 v2, v4 offset:13312
	s_and_saveexec_b64 s[4:5], s[0:1]
	v_lshl_or_b32 v3, v3, 9, v1
	v_add_f32_e32 v4, v70, v16
	ds_write_b32 v3, v4
	s_or_b64 exec, exec, s[4:5]
	v_add_f32_e32 v3, v70, v33
	ds_write_b32 v2, v3 offset:13824
	s_and_saveexec_b64 s[0:1], vcc
	v_add_f32_e32 v2, v70, v17
	ds_write_b32 v1, v2 offset:30208
	s_or_b64 exec, exec, s[0:1]
	v_lshlrev_b32_e32 v1, 4, v0
	v_and_b32_e32 v4, 0x1f0, v1
	v_mov_b32_e32 v5, 0
	v_lshrrev_b32_e32 v1, 5, v0
	v_lshl_add_u64 v[2:3], s[2:3], 0, v[4:5]
	v_add_u32_e32 v6, s16, v1
	s_mov_b32 s2, 0x186a0
	v_cmp_gt_i32_e32 vcc, s2, v6
	s_waitcnt lgkmcnt(0)
	s_barrier
	s_and_saveexec_b64 s[0:1], vcc
	s_cbranch_execz .LBB3_71
	v_lshl_or_b32 v1, v1, 9, v4
	ds_read_b128 v[8:11], v1
	v_ashrrev_i32_e32 v7, 31, v6
	v_lshlrev_b64 v[6:7], 9, v[6:7]
	v_lshl_add_u64 v[6:7], v[2:3], 0, v[6:7]
	s_waitcnt lgkmcnt(0)
	global_store_dwordx4 v[6:7], v[8:11], off sc1

	.amdhsa_kernel _Z7k_layerILb0EEvPKvPKhPKfPKiS7_PKDF16_S5_PvPhPf
		.amdhsa_group_segment_fixed_size 30720
		.amdhsa_private_segment_fixed_size 0
		.amdhsa_kernarg_size 80
		.amdhsa_user_sgpr_count 2
		.amdhsa_user_sgpr_dispatch_ptr 0
		.amdhsa_user_sgpr_queue_ptr 0
		.amdhsa_user_sgpr_kernarg_segment_ptr 1
		.amdhsa_user_sgpr_dispatch_id 0
		.amdhsa_user_sgpr_kernarg_preload_length 0
		.amdhsa_user_sgpr_kernarg_preload_offset 0
		.amdhsa_user_sgpr_private_segment_size 0
		.amdhsa_uses_dynamic_stack 0
		.amdhsa_enable_private_segment 0
		.amdhsa_system_sgpr_workgroup_id_x 1
		.amdhsa_system_sgpr_workgroup_id_y 0
		.amdhsa_system_sgpr_workgroup_id_z 0
		.amdhsa_system_sgpr_workgroup_info 0
		.amdhsa_system_vgpr_workitem_id 0
		.amdhsa_next_free_vgpr 92
		.amdhsa_next_free_sgpr 96
		.amdhsa_accum_offset 92
		.amdhsa_reserve_vcc 1
		.amdhsa_float_round_mode_32 0
		.amdhsa_float_round_mode_16_64 0
		.amdhsa_float_denorm_mode_32 3
		.amdhsa_float_denorm_mode_16_64 3
		.amdhsa_dx10_clamp 1
		.amdhsa_ieee_mode 1
		.amdhsa_fp16_overflow 0
		.amdhsa_tg_split 0
		.amdhsa_exception_fp_ieee_invalid_op 0
		.amdhsa_exception_fp_denorm_src 0
		.amdhsa_exception_fp_ieee_div_zero 0
		.amdhsa_exception_fp_ieee_overflow 0
		.amdhsa_exception_fp_ieee_underflow 0
		.amdhsa_exception_fp_ieee_inexact 0
		.amdhsa_exception_int_div_zero 0
	.end_amdhsa_kernel

.Lfunc_end3:
	.size	_Z7k_layerILb0EEvPKvPKhPKfPKiS7_PKDF16_S5_PvPhPf, .Lfunc_end3-_Z7k_layerILb0EEvPKvPKhPKfPKiS7_PKDF16_S5_PvPhPf
	.set _Z7k_layerILb0EEvPKvPKhPKfPKiS7_PKDF16_S5_PvPhPf.num_vgpr, 92
	.set _Z7k_layerILb0EEvPKvPKhPKfPKiS7_PKDF16_S5_PvPhPf.num_agpr, 0
	.set _Z7k_layerILb0EEvPKvPKhPKfPKiS7_PKDF16_S5_PvPhPf.numbered_sgpr, 28
	.set _Z7k_layerILb0EEvPKvPKhPKfPKiS7_PKDF16_S5_PvPhPf.num_named_barrier, 0
	.set _Z7k_layerILb0EEvPKvPKhPKfPKiS7_PKDF16_S5_PvPhPf.private_seg_size, 0
	.set _Z7k_layerILb0EEvPKvPKhPKfPKiS7_PKDF16_S5_PvPhPf.uses_vcc, 1
	.set _Z7k_layerILb0EEvPKvPKhPKfPKiS7_PKDF16_S5_PvPhPf.uses_flat_scratch, 0
	.set _Z7k_layerILb0EEvPKvPKhPKfPKiS7_PKDF16_S5_PvPhPf.has_dyn_sized_stack, 0
	.set _Z7k_layerILb0EEvPKvPKhPKfPKiS7_PKDF16_S5_PvPhPf.has_recursion, 0
	.set _Z7k_layerILb0EEvPKvPKhPKfPKiS7_PKDF16_S5_PvPhPf.has_indirect_call, 0

amdhsa.kernels:
  - .agpr_count:     0
    .args:
      - .actual_access:  read_only
        .address_space:  global
        .offset:         0
        .size:           8
        .value_kind:     global_buffer
      - .actual_access:  read_only
        .address_space:  global
        .offset:         8
        .size:           8
        .value_kind:     global_buffer
      - .actual_access:  read_only
        .address_space:  global
        .offset:         16
        .size:           8
        .value_kind:     global_buffer
      - .actual_access:  read_only
        .address_space:  global
        .offset:         24
        .size:           8
        .value_kind:     global_buffer
      - .actual_access:  read_only
        .address_space:  global
        .offset:         32
        .size:           8
        .value_kind:     global_buffer
      - .actual_access:  read_only
        .address_space:  global
        .offset:         40
        .size:           8
        .value_kind:     global_buffer
      - .actual_access:  read_only
        .address_space:  global
        .offset:         48
        .size:           8
        .value_kind:     global_buffer
      - .actual_access:  write_only
        .address_space:  global
        .offset:         56
        .size:           8
        .value_kind:     global_buffer
      - .actual_access:  write_only
        .address_space:  global
        .offset:         64
        .size:           8
        .value_kind:     global_buffer
      - .actual_access:  write_only
        .address_space:  global
        .offset:         72
        .size:           8
        .value_kind:     global_buffer
      - .actual_access:  write_only
        .address_space:  global
        .offset:         80
        .size:           8
        .value_kind:     global_buffer
      - .actual_access:  write_only
        .address_space:  global
        .offset:         88
        .size:           8
        .value_kind:     global_buffer
      - .actual_access:  write_only
        .address_space:  global
        .offset:         96
        .size:           8
        .value_kind:     global_buffer
      - .actual_access:  write_only
        .address_space:  global
        .offset:         104
        .size:           8
        .value_kind:     global_buffer
      - .actual_access:  write_only
        .address_space:  global
        .offset:         112
        .size:           8
        .value_kind:     global_buffer
      - .actual_access:  write_only
        .address_space:  global
        .offset:         120
        .size:           8
        .value_kind:     global_buffer
      - .actual_access:  write_only
        .address_space:  global
        .offset:         128
        .size:           8
        .value_kind:     global_buffer
      - .offset:         136
        .size:           4
        .value_kind:     hidden_block_count_x
      - .offset:         140
        .size:           4
        .value_kind:     hidden_block_count_y
      - .offset:         144
        .size:           4
        .value_kind:     hidden_block_count_z
      - .offset:         148
        .size:           2
        .value_kind:     hidden_group_size_x
      - .offset:         150
        .size:           2
        .value_kind:     hidden_group_size_y
      - .offset:         152
        .size:           2
        .value_kind:     hidden_group_size_z
      - .offset:         154
        .size:           2
        .value_kind:     hidden_remainder_x
      - .offset:         156
        .size:           2
        .value_kind:     hidden_remainder_y
      - .offset:         158
        .size:           2
        .value_kind:     hidden_remainder_z
      - .offset:         176
        .size:           8
        .value_kind:     hidden_global_offset_x
      - .offset:         184
        .size:           8
        .value_kind:     hidden_global_offset_y
      - .offset:         192
        .size:           8
        .value_kind:     hidden_global_offset_z
      - .offset:         200
        .size:           2
        .value_kind:     hidden_grid_dims
    .group_segment_fixed_size: 27136
    .kernarg_segment_align: 8
    .kernarg_segment_size: 392
    .language:       OpenCL C
    .language_version:
      - 2
      - 0
    .max_flat_workgroup_size: 1024
    .name:           _Z3k_APKfPKiS2_S0_S0_S0_S0_PDF16_S3_S3_S3_PiS4_PhS5_PfS6_
    .private_segment_fixed_size: 0
    .sgpr_count:     40
    .sgpr_spill_count: 0
    .symbol:         _Z3k_APKfPKiS2_S0_S0_S0_S0_PDF16_S3_S3_S3_PiS4_PhS5_PfS6_.kd
    .uniform_work_group_size: 1
    .uses_dynamic_stack: false
    .vgpr_count:     48
    .vgpr_spill_count: 0
    .wavefront_size: 64
  - .agpr_count:     0
    .args:
      - .actual_access:  read_only
        .address_space:  global
        .offset:         0
        .size:           8
        .value_kind:     global_buffer
      - .actual_access:  read_only
        .address_space:  global
        .offset:         8
        .size:           8
        .value_kind:     global_buffer
      - .actual_access:  write_only
        .address_space:  global
        .offset:         16
        .size:           8
        .value_kind:     global_buffer
      - .actual_access:  write_only
        .address_space:  global
        .offset:         24
        .size:           8
        .value_kind:     global_buffer
      - .actual_access:  read_only
        .address_space:  global
        .offset:         32
        .size:           8
        .value_kind:     global_buffer
      - .actual_access:  read_only
        .address_space:  global
        .offset:         40
        .size:           8
        .value_kind:     global_buffer
    .group_segment_fixed_size: 27720
    .kernarg_segment_align: 8
    .kernarg_segment_size: 48
    .language:       OpenCL C
    .language_version:
      - 2
      - 0
    .max_flat_workgroup_size: 1024
    .name:           _Z3k_BPKiS0_PiS1_PKfPDF16_
    .private_segment_fixed_size: 0
    .sgpr_count:     40
    .sgpr_spill_count: 0
    .symbol:         _Z3k_BPKiS0_PiS1_PKfPDF16_.kd
    .uniform_work_group_size: 1
    .uses_dynamic_stack: false
    .vgpr_count:     60
    .vgpr_spill_count: 0
    .wavefront_size: 64
  - .agpr_count:     0
    .args:
      - .actual_access:  read_only
        .address_space:  global
        .offset:         0
        .size:           8
        .value_kind:     global_buffer
      - .actual_access:  read_only
        .address_space:  global
        .offset:         8
        .size:           8
        .value_kind:     global_buffer
      - .actual_access:  read_only
        .address_space:  global
        .offset:         16
        .size:           8
        .value_kind:     global_buffer
      - .actual_access:  read_only
        .address_space:  global
        .offset:         24
        .size:           8
        .value_kind:     global_buffer
      - .actual_access:  read_only
        .address_space:  global
        .offset:         32
        .size:           8
        .value_kind:     global_buffer
      - .actual_access:  read_only
        .address_space:  global
        .offset:         40
        .size:           8
        .value_kind:     global_buffer
      - .actual_access:  read_only
        .address_space:  global
        .offset:         48
        .size:           8
        .value_kind:     global_buffer
      - .actual_access:  write_only
        .address_space:  global
        .offset:         56
        .size:           8
        .value_kind:     global_buffer
      - .actual_access:  write_only
        .address_space:  global
        .offset:         64
        .size:           8
        .value_kind:     global_buffer
      - .actual_access:  write_only
        .address_space:  global
        .offset:         72
        .size:           8
        .value_kind:     global_buffer
    .group_segment_fixed_size: 30720
    .kernarg_segment_align: 8
    .kernarg_segment_size: 80
    .language:       OpenCL C
    .language_version:
      - 2
      - 0
    .max_flat_workgroup_size: 256
    .name:           _Z7k_layerILb1EEvPKvPKhPKfPKiS7_PKDF16_S5_PvPhPf
    .private_segment_fixed_size: 0
    .sgpr_count:     36
    .sgpr_spill_count: 0
    .symbol:         _Z7k_layerILb1EEvPKvPKhPKfPKiS7_PKDF16_S5_PvPhPf.kd
    .uniform_work_group_size: 1
    .uses_dynamic_stack: false
    .vgpr_count:     96
    .vgpr_spill_count: 0
    .wavefront_size: 64
  - .agpr_count:     0
    .args:
      - .actual_access:  read_only
        .address_space:  global
        .offset:         0
        .size:           8
        .value_kind:     global_buffer
      - .actual_access:  read_only
        .address_space:  global
        .offset:         8
        .size:           8
        .value_kind:     global_buffer
      - .actual_access:  read_only
        .address_space:  global
        .offset:         16
        .size:           8
        .value_kind:     global_buffer
      - .actual_access:  read_only
        .address_space:  global
        .offset:         24
        .size:           8
        .value_kind:     global_buffer
      - .actual_access:  read_only
        .address_space:  global
        .offset:         32
        .size:           8
        .value_kind:     global_buffer
      - .actual_access:  read_only
        .address_space:  global
        .offset:         40
        .size:           8
        .value_kind:     global_buffer
      - .actual_access:  read_only
        .address_space:  global
        .offset:         48
        .size:           8
        .value_kind:     global_buffer
      - .actual_access:  write_only
        .address_space:  global
        .offset:         56
        .size:           8
        .value_kind:     global_buffer
      - .actual_access:  read_only
        .address_space:  global
        .offset:         64
        .size:           8
        .value_kind:     global_buffer
      - .actual_access:  read_only
        .address_space:  global
        .offset:         72
        .size:           8
        .value_kind:     global_buffer
    .group_segment_fixed_size: 30720
    .kernarg_segment_align: 8
    .kernarg_segment_size: 80
    .language:       OpenCL C
    .language_version:
      - 2
      - 0
    .max_flat_workgroup_size: 256
    .name:           _Z7k_layerILb0EEvPKvPKhPKfPKiS7_PKDF16_S5_PvPhPf
    .private_segment_fixed_size: 0
    .sgpr_count:     34
    .sgpr_spill_count: 0
    .symbol:         _Z7k_layerILb0EEvPKvPKhPKfPKiS7_PKDF16_S5_PvPhPf.kd
    .uniform_work_group_size: 1
    .uses_dynamic_stack: false
    .vgpr_count:     92
    .vgpr_spill_count: 0
    .wavefront_size: 64
